# baseline (speedup 1.0000x reference)
_Z13expert_kernelPKfS0_PKcPf:
	s_load_dwordx2 s[20:21], s[0:1], 0x10
	s_load_dwordx2 s[22:23], s[0:1], 0x8
	s_load_dwordx2 s[18:19], s[0:1], 0x18
	s_mov_b32 s64, s2
	v_and_b32_e32 v92, 63, v0
	v_readfirstlane_b32 s26, v0
	v_cmp_gt_u32_e64 s[12:13], 20, v0
	v_lshlrev_b32_e32 v3, 2, v92
	v_cmp_gt_u32_e64 s[30:31], 20, v92
	v_mov_b32_e32 v132, 0
	v_mov_b32_e32 v133, 0
	v_mov_b32_e32 v134, 0
	v_mov_b32_e32 v135, 0
	v_mov_b32_e32 v136, 0
	v_mov_b32_e32 v137, 0
	v_mov_b32_e32 v138, 0
	v_mov_b32_e32 v139, 0
	s_lshr_b32 s27, s26, 6
	s_waitcnt lgkmcnt(0)
	s_add_u32 s32, s20, 0x3000000
	s_addc_u32 s33, s21, 0
	s_add_u32 s34, s32, 0xcf0
	s_addc_u32 s35, s33, 0
	s_add_u32 s36, s32, 0x19e0
	s_addc_u32 s37, s33, 0
	global_load_dword v100, v3, s[32:33]
	global_load_dword v101, v3, s[32:33] offset:1104
	global_load_dword v102, v3, s[32:33] offset:2208
	global_load_dword v103, v3, s[34:35]
	global_load_dword v104, v3, s[34:35] offset:1104
	global_load_dword v105, v3, s[34:35] offset:2208
	global_load_dword v106, v3, s[36:37]
	global_load_dword v107, v3, s[36:37] offset:1104
	global_load_dword v108, v3, s[32:33] offset:256
	global_load_dword v109, v3, s[32:33] offset:1360
	global_load_dword v110, v3, s[32:33] offset:2464
	global_load_dword v111, v3, s[34:35] offset:256
	global_load_dword v112, v3, s[34:35] offset:1360
	global_load_dword v113, v3, s[34:35] offset:2464
	global_load_dword v114, v3, s[36:37] offset:256
	global_load_dword v115, v3, s[36:37] offset:1360
	global_load_dword v116, v3, s[32:33] offset:512
	global_load_dword v117, v3, s[32:33] offset:1616
	global_load_dword v118, v3, s[32:33] offset:2720
	global_load_dword v119, v3, s[34:35] offset:512
	global_load_dword v120, v3, s[34:35] offset:1616
	global_load_dword v121, v3, s[34:35] offset:2720
	global_load_dword v122, v3, s[36:37] offset:512
	global_load_dword v123, v3, s[36:37] offset:1616
	global_load_dword v124, v3, s[32:33] offset:768
	global_load_dword v125, v3, s[32:33] offset:1872
	global_load_dword v126, v3, s[32:33] offset:2976
	global_load_dword v127, v3, s[34:35] offset:768
	global_load_dword v128, v3, s[34:35] offset:1872
	global_load_dword v129, v3, s[34:35] offset:2976
	global_load_dword v130, v3, s[36:37] offset:768
	global_load_dword v131, v3, s[36:37] offset:1872
	s_and_saveexec_b64 s[38:39], s[30:31]
	global_load_dword v132, v3, s[32:33] offset:1024
	global_load_dword v133, v3, s[32:33] offset:2128
	global_load_dword v134, v3, s[32:33] offset:3232
	global_load_dword v135, v3, s[34:35] offset:1024
	global_load_dword v136, v3, s[34:35] offset:2128
	global_load_dword v137, v3, s[34:35] offset:3232
	global_load_dword v138, v3, s[36:37] offset:1024
	global_load_dword v139, v3, s[36:37] offset:2128
	s_mov_b64 exec, s[38:39]
	s_waitcnt vmcnt(0)
	v_add3_u32 v140, v100, v101, v102
	v_add3_u32 v140, v140, v103, v104
	v_add3_u32 v140, v140, v105, v106
	v_add_u32_e32 v140, v140, v107
	v_add3_u32 v141, v108, v109, v110
	v_add3_u32 v141, v141, v111, v112
	v_add3_u32 v141, v141, v113, v114
	v_add_u32_e32 v141, v141, v115
	v_add3_u32 v142, v116, v117, v118
	v_add3_u32 v142, v142, v119, v120
	v_add3_u32 v142, v142, v121, v122
	v_add_u32_e32 v142, v142, v123
	v_add3_u32 v143, v124, v125, v126
	v_add3_u32 v143, v143, v127, v128
	v_add3_u32 v143, v143, v129, v130
	v_add_u32_e32 v143, v143, v131
	v_add3_u32 v144, v132, v133, v134
	v_add3_u32 v144, v144, v135, v136
	v_add3_u32 v144, v144, v137, v138
	v_add_u32_e32 v144, v144, v139
	v_add_u32_e32 v145, 0x7f, v140
	v_add_u32_e32 v146, 0x7f, v141
	v_add_u32_e32 v147, 0x7f, v142
	v_add_u32_e32 v148, 0x7f, v143
	v_add_u32_e32 v149, 0x7f, v144
	v_lshrrev_b32_e32 v145, 7, v145
	v_lshrrev_b32_e32 v146, 7, v146
	v_lshrrev_b32_e32 v147, 7, v147
	v_lshrrev_b32_e32 v148, 7, v148
	v_lshrrev_b32_e32 v149, 7, v149
	v_mov_b32_e32 v150, v145
	v_mov_b32_e32 v151, v146
	v_mov_b32_e32 v152, v147
	v_mov_b32_e32 v153, v148
	v_mov_b32_e32 v154, v149
	v_add_u32_dpp v150, v150, v150 row_shr:1 row_mask:0xf bank_mask:0xf
	v_add_u32_dpp v151, v151, v151 row_shr:1 row_mask:0xf bank_mask:0xf
	v_add_u32_dpp v152, v152, v152 row_shr:1 row_mask:0xf bank_mask:0xf
	v_add_u32_dpp v153, v153, v153 row_shr:1 row_mask:0xf bank_mask:0xf
	v_add_u32_dpp v154, v154, v154 row_shr:1 row_mask:0xf bank_mask:0xf
	v_add_u32_dpp v150, v150, v150 row_shr:2 row_mask:0xf bank_mask:0xf
	v_add_u32_dpp v151, v151, v151 row_shr:2 row_mask:0xf bank_mask:0xf
	v_add_u32_dpp v152, v152, v152 row_shr:2 row_mask:0xf bank_mask:0xf
	v_add_u32_dpp v153, v153, v153 row_shr:2 row_mask:0xf bank_mask:0xf
	v_add_u32_dpp v154, v154, v154 row_shr:2 row_mask:0xf bank_mask:0xf
	v_add_u32_dpp v150, v150, v150 row_shr:4 row_mask:0xf bank_mask:0xf
	v_add_u32_dpp v151, v151, v151 row_shr:4 row_mask:0xf bank_mask:0xf
	v_add_u32_dpp v152, v152, v152 row_shr:4 row_mask:0xf bank_mask:0xf
	v_add_u32_dpp v153, v153, v153 row_shr:4 row_mask:0xf bank_mask:0xf
	v_add_u32_dpp v154, v154, v154 row_shr:4 row_mask:0xf bank_mask:0xf
	v_add_u32_dpp v150, v150, v150 row_shr:8 row_mask:0xf bank_mask:0xf
	v_add_u32_dpp v151, v151, v151 row_shr:8 row_mask:0xf bank_mask:0xf
	v_add_u32_dpp v152, v152, v152 row_shr:8 row_mask:0xf bank_mask:0xf
	v_add_u32_dpp v153, v153, v153 row_shr:8 row_mask:0xf bank_mask:0xf
	v_add_u32_dpp v154, v154, v154 row_shr:8 row_mask:0xf bank_mask:0xf
	v_add_u32_dpp v150, v150, v150 row_bcast:15 row_mask:0xa bank_mask:0xf
	v_add_u32_dpp v151, v151, v151 row_bcast:15 row_mask:0xa bank_mask:0xf
	v_add_u32_dpp v152, v152, v152 row_bcast:15 row_mask:0xa bank_mask:0xf
	v_add_u32_dpp v153, v153, v153 row_bcast:15 row_mask:0xa bank_mask:0xf
	v_add_u32_dpp v154, v154, v154 row_bcast:15 row_mask:0xa bank_mask:0xf
	v_add_u32_dpp v150, v150, v150 row_bcast:31 row_mask:0xc bank_mask:0xf
	v_add_u32_dpp v151, v151, v151 row_bcast:31 row_mask:0xc bank_mask:0xf
	v_add_u32_dpp v152, v152, v152 row_bcast:31 row_mask:0xc bank_mask:0xf
	v_add_u32_dpp v153, v153, v153 row_bcast:31 row_mask:0xc bank_mask:0xf
	v_add_u32_dpp v154, v154, v154 row_bcast:31 row_mask:0xc bank_mask:0xf
	s_nop 1
	v_readlane_b32 s40, v150, 63
	v_readlane_b32 s41, v151, 63
	v_readlane_b32 s42, v152, 63
	v_readlane_b32 s43, v153, 63
	v_readlane_b32 s44, v154, 63
	s_nop 3
	s_mov_b32 s45, 0
	s_mov_b32 s46, s40
	s_add_u32 s47, s46, s41
	s_add_u32 s48, s47, s42
	s_add_u32 s49, s48, s43
	v_sub_u32_e32 v32, v150, v145
	v_sub_u32_e32 v33, v151, v146
	v_sub_u32_e32 v34, v152, v147
	v_sub_u32_e32 v35, v153, v148
	v_sub_u32_e32 v36, v154, v149
	v_add_u32_e32 v32, s45, v32
	v_add_u32_e32 v33, s46, v33
	v_add_u32_e32 v34, s47, v34
	v_add_u32_e32 v35, s48, v35
	v_add_u32_e32 v36, s49, v36
	v_add_u32_e32 v150, v32, v145
	v_add_u32_e32 v151, v33, v146
	v_add_u32_e32 v152, v34, v147
	v_add_u32_e32 v153, v35, v148
	v_add_u32_e32 v154, v36, v149
	v_cmp_ge_u32_e64 s[52:53], s64, v32
	v_cmp_lt_u32_e64 s[54:55], s64, v150
	s_nop 0
	s_and_b64 s[66:67], s[52:53], s[54:55]
	v_cmp_ge_u32_e64 s[52:53], s64, v33
	v_cmp_lt_u32_e64 s[54:55], s64, v151
	s_nop 0
	s_and_b64 s[68:69], s[52:53], s[54:55]
	v_cmp_ge_u32_e64 s[52:53], s64, v34
	v_cmp_lt_u32_e64 s[54:55], s64, v152
	s_nop 0
	s_and_b64 s[70:71], s[52:53], s[54:55]
	v_cmp_ge_u32_e64 s[52:53], s64, v35
	v_cmp_lt_u32_e64 s[54:55], s64, v153
	s_nop 0
	s_and_b64 s[72:73], s[52:53], s[54:55]
	v_cmp_ge_u32_e64 s[52:53], s64, v36
	v_cmp_lt_u32_e64 s[54:55], s64, v154
	s_nop 0
	s_and_b64 s[74:75], s[52:53], s[54:55]
	v_mov_b32_e32 v20, 0
	v_mov_b32_e32 v21, 0
	v_mov_b32_e32 v22, 0
	v_mov_b32_e32 v23, 0
	v_mov_b32_e32 v24, 0
	v_mov_b32_e32 v25, 0
	v_mov_b32_e32 v26, 0
	v_mov_b32_e32 v27, 0
	v_mov_b32_e32 v28, 0
	v_mov_b32_e32 v29, 0
	v_mov_b32_e32 v30, 0
	v_cndmask_b32_e64 v20, v20, v100, s[66:67]
	v_cndmask_b32_e64 v21, v21, v101, s[66:67]
	v_cndmask_b32_e64 v22, v22, v102, s[66:67]
	v_cndmask_b32_e64 v23, v23, v103, s[66:67]
	v_cndmask_b32_e64 v24, v24, v104, s[66:67]
	v_cndmask_b32_e64 v25, v25, v105, s[66:67]
	v_cndmask_b32_e64 v26, v26, v106, s[66:67]
	v_cndmask_b32_e64 v27, v27, v107, s[66:67]
	v_cndmask_b32_e64 v28, v28, v140, s[66:67]
	v_cndmask_b32_e64 v29, v29, v32, s[66:67]
	v_cndmask_b32_e64 v30, v30, v92, s[66:67]
	v_cndmask_b32_e64 v20, v20, v108, s[68:69]
	v_cndmask_b32_e64 v21, v21, v109, s[68:69]
	v_cndmask_b32_e64 v22, v22, v110, s[68:69]
	v_cndmask_b32_e64 v23, v23, v111, s[68:69]
	v_cndmask_b32_e64 v24, v24, v112, s[68:69]
	v_cndmask_b32_e64 v25, v25, v113, s[68:69]
	v_cndmask_b32_e64 v26, v26, v114, s[68:69]
	v_cndmask_b32_e64 v27, v27, v115, s[68:69]
	v_cndmask_b32_e64 v28, v28, v141, s[68:69]
	v_cndmask_b32_e64 v29, v29, v33, s[68:69]
	v_add_u32_e32 v31, 64, v92
	v_cndmask_b32_e64 v30, v30, v31, s[68:69]
	v_cndmask_b32_e64 v20, v20, v116, s[70:71]
	v_cndmask_b32_e64 v21, v21, v117, s[70:71]
	v_cndmask_b32_e64 v22, v22, v118, s[70:71]
	v_cndmask_b32_e64 v23, v23, v119, s[70:71]
	v_cndmask_b32_e64 v24, v24, v120, s[70:71]
	v_cndmask_b32_e64 v25, v25, v121, s[70:71]
	v_cndmask_b32_e64 v26, v26, v122, s[70:71]
	v_cndmask_b32_e64 v27, v27, v123, s[70:71]
	v_cndmask_b32_e64 v28, v28, v142, s[70:71]
	v_cndmask_b32_e64 v29, v29, v34, s[70:71]
	v_add_u32_e32 v31, 128, v92
	v_cndmask_b32_e64 v30, v30, v31, s[70:71]
	v_cndmask_b32_e64 v20, v20, v124, s[72:73]
	v_cndmask_b32_e64 v21, v21, v125, s[72:73]
	v_cndmask_b32_e64 v22, v22, v126, s[72:73]
	v_cndmask_b32_e64 v23, v23, v127, s[72:73]
	v_cndmask_b32_e64 v24, v24, v128, s[72:73]
	v_cndmask_b32_e64 v25, v25, v129, s[72:73]
	v_cndmask_b32_e64 v26, v26, v130, s[72:73]
	v_cndmask_b32_e64 v27, v27, v131, s[72:73]
	v_cndmask_b32_e64 v28, v28, v143, s[72:73]
	v_cndmask_b32_e64 v29, v29, v35, s[72:73]
	v_add_u32_e32 v31, 192, v92
	v_cndmask_b32_e64 v30, v30, v31, s[72:73]
	v_cndmask_b32_e64 v20, v20, v132, s[74:75]
	v_cndmask_b32_e64 v21, v21, v133, s[74:75]
	v_cndmask_b32_e64 v22, v22, v134, s[74:75]
	v_cndmask_b32_e64 v23, v23, v135, s[74:75]
	v_cndmask_b32_e64 v24, v24, v136, s[74:75]
	v_cndmask_b32_e64 v25, v25, v137, s[74:75]
	v_cndmask_b32_e64 v26, v26, v138, s[74:75]
	v_cndmask_b32_e64 v27, v27, v139, s[74:75]
	v_cndmask_b32_e64 v28, v28, v144, s[74:75]
	v_cndmask_b32_e64 v29, v29, v36, s[74:75]
	v_add_u32_e32 v31, 256, v92
	v_cndmask_b32_e64 v30, v30, v31, s[74:75]
	s_or_b64 s[66:67], s[66:67], s[68:69]
	s_or_b64 s[70:71], s[70:71], s[72:73]
	s_or_b64 s[66:67], s[66:67], s[74:75]
	s_or_b64 s[66:67], s[66:67], s[70:71]
	s_cmp_eq_u64 s[66:67], 0
	s_cbranch_scc1 .LBB3_39
	s_ff1_i32_b64 s76, s[66:67]
	s_nop 0
	v_readlane_b32 s78, v20, s76
	v_readlane_b32 s79, v21, s76
	v_readlane_b32 s80, v22, s76
	v_readlane_b32 s81, v23, s76
	v_readlane_b32 s82, v24, s76
	v_readlane_b32 s83, v25, s76
	v_readlane_b32 s84, v26, s76
	v_readlane_b32 s85, v27, s76
	v_readlane_b32 s86, v28, s76
	v_readlane_b32 s87, v29, s76
	v_readlane_b32 s88, v30, s76
	s_nop 3
	s_add_u32 s79, s79, s78
	s_add_u32 s80, s80, s79
	s_add_u32 s81, s81, s80
	s_add_u32 s82, s82, s81
	s_add_u32 s83, s83, s82
	s_add_u32 s84, s84, s83
	s_sub_u32 s87, s64, s87
	s_nop 1
	v_mov_b32_e32 v6, s87
	v_mov_b32_e32 v7, s86
	v_mov_b32_e32 v12, s78
	v_mov_b32_e32 v13, s79
	v_mov_b32_e32 v10, s80
	v_mov_b32_e32 v11, s81
	v_mov_b32_e32 v8, s82
	v_mov_b32_e32 v9, s83
	v_mov_b32_e32 v1, s84
	s_mov_b32 s2, s88
	s_mov_b32 s28, 0
	s_cmp_lt_u32 s2, 23
	s_mov_b32 s0, s2
	s_cbranch_scc1 .LBB3_29
	s_movk_i32 s4, 0xffe8
	s_mov_b32 s1, 22
	s_mov_b32 s0, s2

amdhsa.kernels:
  - .agpr_count:     0
    .args:
      - .actual_access:  read_only
        .address_space:  global
        .offset:         0
        .size:           8
        .value_kind:     global_buffer
      - .actual_access:  read_only
        .address_space:  global
        .offset:         8
        .size:           8
        .value_kind:     global_buffer
      - .actual_access:  read_only
        .address_space:  global
        .offset:         16
        .size:           8
        .value_kind:     global_buffer
      - .actual_access:  read_only
        .address_space:  global
        .offset:         24
        .size:           8
        .value_kind:     global_buffer
      - .actual_access:  write_only
        .address_space:  global
        .offset:         32
        .size:           8
        .value_kind:     global_buffer
    .group_segment_fixed_size: 0
    .kernarg_segment_align: 8
    .kernarg_segment_size: 40
    .language:       OpenCL C
    .language_version:
      - 2
      - 0
    .max_flat_workgroup_size: 256
    .name:           _Z11prep_kernelPKfS0_S0_S0_Pc
    .private_segment_fixed_size: 0
    .sgpr_count:     30
    .sgpr_spill_count: 0
    .symbol:         _Z11prep_kernelPKfS0_S0_S0_Pc.kd
    .uniform_work_group_size: 1
    .uses_dynamic_stack: false
    .vgpr_count:     20
    .vgpr_spill_count: 0
    .wavefront_size: 64
  - .agpr_count:     0
    .args:
      - .address_space:  global
        .offset:         0
        .size:           8
        .value_kind:     global_buffer
      - .actual_access:  read_only
        .address_space:  global
        .offset:         8
        .size:           8
        .value_kind:     global_buffer
      - .actual_access:  read_only
        .address_space:  global
        .offset:         16
        .size:           8
        .value_kind:     global_buffer
      - .address_space:  global
        .offset:         24
        .size:           8
        .value_kind:     global_buffer
      - .actual_access:  write_only
        .address_space:  global
        .offset:         32
        .size:           8
        .value_kind:     global_buffer
      - .address_space:  global
        .offset:         40
        .size:           8
        .value_kind:     global_buffer
    .group_segment_fixed_size: 133120
    .kernarg_segment_align: 8
    .kernarg_segment_size: 48
    .language:       OpenCL C
    .language_version:
      - 2
      - 0
    .max_flat_workgroup_size: 512
    .name:           _Z13router_kernelPKfS0_S0_PcPfS1_
    .private_segment_fixed_size: 0
    .sgpr_count:     106
    .sgpr_spill_count: 7
    .symbol:         _Z13router_kernelPKfS0_S0_PcPfS1_.kd
    .uniform_work_group_size: 1
    .uses_dynamic_stack: false
    .vgpr_count:     239
    .vgpr_spill_count: 0
    .wavefront_size: 64
  - .agpr_count:     0
    .args:
      - .address_space:  global
        .offset:         0
        .size:           8
        .value_kind:     global_buffer
    .group_segment_fixed_size: 20
    .kernarg_segment_align: 8
    .kernarg_segment_size: 8
    .language:       OpenCL C
    .language_version:
      - 2
      - 0
    .max_flat_workgroup_size: 320
    .name:           _Z11plan_kernelPc
    .private_segment_fixed_size: 0
    .sgpr_count:     16
    .sgpr_spill_count: 0
    .symbol:         _Z11plan_kernelPc.kd
    .uniform_work_group_size: 1
    .uses_dynamic_stack: false
    .vgpr_count:     20
    .vgpr_spill_count: 0
    .wavefront_size: 64
  - .agpr_count:     96
    .args:
      - .actual_access:  read_only
        .address_space:  global
        .offset:         0
        .size:           8
        .value_kind:     global_buffer
      - .actual_access:  read_only
        .address_space:  global
        .offset:         8
        .size:           8
        .value_kind:     global_buffer
      - .address_space:  global
        .offset:         16
        .size:           8
        .value_kind:     global_buffer
      - .actual_access:  write_only
        .address_space:  global
        .offset:         24
        .size:           8
        .value_kind:     global_buffer
    .group_segment_fixed_size: 78784
    .kernarg_segment_align: 8
    .kernarg_segment_size: 32
    .language:       OpenCL C
    .language_version:
      - 2
      - 0
    .max_flat_workgroup_size: 256
    .name:           _Z13expert_kernelPKfS0_PKcPf
    .private_segment_fixed_size: 0
    .sgpr_count:     95
    .sgpr_spill_count: 0
    .symbol:         _Z13expert_kernelPKfS0_PKcPf.kd
    .uniform_work_group_size: 1
    .uses_dynamic_stack: false
    .vgpr_count:     256
    .vgpr_spill_count: 0
    .wavefront_size: 64
